# grid barrier: pollers wait on the top-level arrival counter reaching (gen+1)*nx instead of a separate generation word; last leader's extra atomic removed
# speedup vs baseline: 1.0040x; 1.0040x over previous
; __device__ __forceinline__ unsigned xb_ld(unsigned* p)              { return __hip_atomic_load(p, __ATOMIC_RELAXED, __HIP_MEMORY_SCOPE_AGENT); }
; __device__ __forceinline__ unsigned xb_add(unsigned* p, unsigned v) { return __hip_atomic_fetch_add(p, v, __ATOMIC_RELAXED, __HIP_MEMORY_SCOPE_AGENT); }
; #define XB_SPIN(cond, bar) do { unsigned _sp = 0; while (cond) { __builtin_amdgcn_s_sleep(1); \
;     if ((++_sp & 255u) == 0u) { if (xb_ld(&(bar)[XB_TMO])) break; if (_sp > XB_SPIN_CAP) { atomicAdd(&(bar)[XB_TMO], 1u); break; } } } } while (0)
; __device__ __forceinline__ void xcd_barrier(const XcdBarrier& b, const int wv) {
;     ...
;         const unsigned old = xb_add(&bar[XB_XSUB(bx)], 1u);
;         const unsigned gen = old / nloc;
;         if (old + 1u == (gen + 1u) * nloc) {
;             __builtin_amdgcn_fence(__ATOMIC_RELEASE, "agent");
;             asm volatile("s_waitcnt vmcnt(0)" ::: "memory");
;             const unsigned og = xb_add(&bar[XB_TOP], 1u);
;             const unsigned tg = og / nx;
;             __builtin_amdgcn_fence(__ATOMIC_ACQUIRE, "agent");
;             if (og + 1u == (tg + 1u) * nx) xb_add(&bar[XB_TOPGEN], 1u);
;             else XB_SPIN(xb_ld(&bar[XB_TOPGEN]) == tg, bar);
;             asm volatile("s_waitcnt vmcnt(0)" ::: "memory");
;         } else {
;             __builtin_amdgcn_fence(__ATOMIC_ACQUIRE, "agent");
;             XB_SPIN(xb_ld(&bar[XB_TOPGEN]) == gen, bar);
.LBB0_171:
	s_or_b64 exec, exec, s[8:9]
	v_cvt_f32_u32_e32 v5, v3
	s_waitcnt vmcnt(0)
	v_readfirstlane_b32 s6, v4
	v_sub_u32_e32 v4, 0, v3
	v_rcp_iflag_f32_e32 v5, v5
	v_add_u32_e32 v6, s6, v2
	v_mul_f32_e32 v5, 0x4f7ffffe, v5
	v_cvt_u32_f32_e32 v5, v5
	v_mul_lo_u32 v2, v4, v5
	v_mul_hi_u32 v2, v5, v2
	v_add_u32_e32 v2, v5, v2
	v_mul_hi_u32 v2, v6, v2
	v_mul_lo_u32 v4, v2, v3
	v_sub_u32_e32 v4, v6, v4
	v_add_u32_e32 v5, 1, v2
	v_cmp_ge_u32_e32 vcc, v4, v3
	s_nop 1
	v_cndmask_b32_e32 v2, v2, v5, vcc
	v_sub_u32_e32 v5, v4, v3
	v_cndmask_b32_e32 v4, v4, v5, vcc
	v_add_u32_e32 v5, 1, v2
	v_cmp_ge_u32_e32 vcc, v4, v3
	v_add_u32_e32 v4, 1, v6
	s_nop 0
	v_cndmask_b32_e32 v2, v2, v5, vcc
	v_mul_lo_u32 v5, v3, v2
	v_add_u32_e32 v3, v5, v3
	v_cmp_ne_u32_e32 vcc, v4, v3
	s_and_saveexec_b64 s[6:7], vcc
	s_xor_b64 s[6:7], exec, s[6:7]
	s_cbranch_execz .LBB0_185
	s_waitcnt lgkmcnt(0)
	v_add_u32_e32 v4, 1, v2
	v_mul_lo_u32 v4, v4, v1
	v_mov_b32_e32 v1, 0x3000
	buffer_inv sc1
	global_load_dword v1, v1, s[4:5] offset:1024 sc1
	s_add_u32 s10, s4, 0x3400
	s_addc_u32 s11, s5, 0
	s_waitcnt vmcnt(0)
	v_cmp_lt_u32_e32 vcc, v1, v4
	s_and_saveexec_b64 s[8:9], vcc
	s_cbranch_execz .LBB0_184
	s_mov_b32 s22, 1
	s_mov_b64 s[12:13], 0
	v_mov_b32_e32 v1, 0
	s_branch .LBB0_175

; __device__ __forceinline__ unsigned xb_ld(unsigned* p)              { return __hip_atomic_load(p, __ATOMIC_RELAXED, __HIP_MEMORY_SCOPE_AGENT); }
; #define XB_SPIN(cond, bar) do { unsigned _sp = 0; while (cond) { __builtin_amdgcn_s_sleep(1); \
;     if ((++_sp & 255u) == 0u) { if (xb_ld(&(bar)[XB_TMO])) break; if (_sp > XB_SPIN_CAP) { atomicAdd(&(bar)[XB_TMO], 1u); break; } } } } while (0)
; __device__ __forceinline__ void xcd_barrier(const XcdBarrier& b, const int wv) {
;     ...
;             else XB_SPIN(xb_ld(&bar[XB_TOPGEN]) == tg, bar);
;             asm volatile("s_waitcnt vmcnt(0)" ::: "memory");
;         } else {
;             __builtin_amdgcn_fence(__ATOMIC_ACQUIRE, "agent");
;             XB_SPIN(xb_ld(&bar[XB_TOPGEN]) == gen, bar);
.LBB0_177:
	global_load_dword v3, v1, s[10:11] sc1
	s_add_i32 s22, s22, 1
	s_mov_b64 s[18:19], -1
	s_waitcnt vmcnt(0)
	v_cmp_ge_u32_e32 vcc, v3, v4
	s_orn2_b64 s[16:17], vcc, exec
	s_branch .LBB0_174

; __device__ __forceinline__ unsigned xb_ld(unsigned* p)              { return __hip_atomic_load(p, __ATOMIC_RELAXED, __HIP_MEMORY_SCOPE_AGENT); }
; __device__ __forceinline__ unsigned xb_add(unsigned* p, unsigned v) { return __hip_atomic_fetch_add(p, v, __ATOMIC_RELAXED, __HIP_MEMORY_SCOPE_AGENT); }
; #define XB_SPIN(cond, bar) do { unsigned _sp = 0; while (cond) { __builtin_amdgcn_s_sleep(1); \
;     if ((++_sp & 255u) == 0u) { if (xb_ld(&(bar)[XB_TMO])) break; if (_sp > XB_SPIN_CAP) { atomicAdd(&(bar)[XB_TMO], 1u); break; } } } } while (0)
; __device__ __forceinline__ void xcd_barrier(const XcdBarrier& b, const int wv) {
;     ...
;         const unsigned old = xb_add(&bar[XB_XSUB(bx)], 1u);
;         const unsigned gen = old / nloc;
;         if (old + 1u == (gen + 1u) * nloc) {
;             __builtin_amdgcn_fence(__ATOMIC_RELEASE, "agent");
;             asm volatile("s_waitcnt vmcnt(0)" ::: "memory");
;             const unsigned og = xb_add(&bar[XB_TOP], 1u);
;             const unsigned tg = og / nx;
;             __builtin_amdgcn_fence(__ATOMIC_ACQUIRE, "agent");
;             if (og + 1u == (tg + 1u) * nx) xb_add(&bar[XB_TOPGEN], 1u);
;             else XB_SPIN(xb_ld(&bar[XB_TOPGEN]) == tg, bar);
;             asm volatile("s_waitcnt vmcnt(0)" ::: "memory");
.LBB0_188:
	s_or_b64 exec, exec, s[8:9]
	v_cvt_f32_u32_e32 v4, v1
	s_waitcnt vmcnt(0)
	v_readfirstlane_b32 s6, v3
	s_add_u32 s8, s4, 0x3400
	s_addc_u32 s9, s5, 0
	v_rcp_iflag_f32_e32 v4, v4
	v_add_u32_e32 v2, s6, v2
	s_mov_b64 s[10:11], 0
	buffer_inv sc1
	v_mul_f32_e32 v3, 0x4f7ffffe, v4
	v_cvt_u32_f32_e32 v3, v3
	v_sub_u32_e32 v4, 0, v1
	v_mul_lo_u32 v4, v4, v3
	v_mul_hi_u32 v4, v3, v4
	v_add_u32_e32 v3, v3, v4
	v_mul_hi_u32 v3, v2, v3
	v_mul_lo_u32 v4, v3, v1
	v_sub_u32_e32 v4, v2, v4
	v_add_u32_e32 v5, 1, v3
	v_cmp_ge_u32_e32 vcc, v4, v1
	v_add_u32_e32 v2, 1, v2
	s_nop 0
	v_cndmask_b32_e32 v3, v3, v5, vcc
	v_sub_u32_e32 v5, v4, v1
	v_cndmask_b32_e32 v4, v4, v5, vcc
	v_add_u32_e32 v5, 1, v3
	v_cmp_ge_u32_e32 vcc, v4, v1
	s_nop 1
	v_cndmask_b32_e32 v4, v3, v5, vcc
	v_mul_lo_u32 v3, v1, v4
	v_add_u32_e32 v1, v3, v1
	v_cmp_ne_u32_e32 vcc, v2, v1
	v_mov_b32_e32 v5, v1
	v_mov_b64_e32 v[2:3], s[8:9]
	s_and_saveexec_b64 s[6:7], vcc
	s_cbranch_execz .LBB0_202
	v_mov_b32_e32 v1, 0
	global_load_dword v2, v1, s[8:9] sc1
	s_mov_b64 s[14:15], 0
	s_waitcnt vmcnt(0)
	v_cmp_lt_u32_e32 vcc, v2, v5
	s_and_saveexec_b64 s[12:13], vcc
	s_cbranch_execz .LBB0_201
	s_add_u32 s10, s4, 0x200
	s_addc_u32 s11, s5, 0
	s_mov_b32 s22, 1
	s_mov_b64 s[4:5], 0
	s_branch .LBB0_192

; __device__ __forceinline__ unsigned xb_ld(unsigned* p)              { return __hip_atomic_load(p, __ATOMIC_RELAXED, __HIP_MEMORY_SCOPE_AGENT); }
; #define XB_SPIN(cond, bar) do { unsigned _sp = 0; while (cond) { __builtin_amdgcn_s_sleep(1); \
;     if ((++_sp & 255u) == 0u) { if (xb_ld(&(bar)[XB_TMO])) break; if (_sp > XB_SPIN_CAP) { atomicAdd(&(bar)[XB_TMO], 1u); break; } } } } while (0)
; __device__ __forceinline__ void xcd_barrier(const XcdBarrier& b, const int wv) {
;     ...
;             else XB_SPIN(xb_ld(&bar[XB_TOPGEN]) == tg, bar);
.LBB0_194:
	global_load_dword v2, v1, s[8:9] sc1
	s_add_i32 s22, s22, 1
	s_mov_b64 s[16:17], -1
	s_waitcnt vmcnt(0)
	v_cmp_ge_u32_e32 vcc, v2, v5
	s_orn2_b64 s[20:21], vcc, exec
	s_branch .LBB0_191

; __device__ __forceinline__ unsigned xb_ld(unsigned* p)              { return __hip_atomic_load(p, __ATOMIC_RELAXED, __HIP_MEMORY_SCOPE_AGENT); }
; __device__ __forceinline__ unsigned xb_add(unsigned* p, unsigned v) { return __hip_atomic_fetch_add(p, v, __ATOMIC_RELAXED, __HIP_MEMORY_SCOPE_AGENT); }
; #define XB_SPIN(cond, bar) do { unsigned _sp = 0; while (cond) { __builtin_amdgcn_s_sleep(1); \
;     if ((++_sp & 255u) == 0u) { if (xb_ld(&(bar)[XB_TMO])) break; if (_sp > XB_SPIN_CAP) { atomicAdd(&(bar)[XB_TMO], 1u); break; } } } } while (0)
; __device__ __forceinline__ void xcd_barrier(const XcdBarrier& b, const int wv) {
;     ...
;         const unsigned old = xb_add(&bar[XB_XSUB(bx)], 1u);
;         const unsigned gen = old / nloc;
;         if (old + 1u == (gen + 1u) * nloc) {
;             __builtin_amdgcn_fence(__ATOMIC_RELEASE, "agent");
;             asm volatile("s_waitcnt vmcnt(0)" ::: "memory");
;             const unsigned og = xb_add(&bar[XB_TOP], 1u);
;             const unsigned tg = og / nx;
;             __builtin_amdgcn_fence(__ATOMIC_ACQUIRE, "agent");
;             if (og + 1u == (tg + 1u) * nx) xb_add(&bar[XB_TOPGEN], 1u);
;             else XB_SPIN(xb_ld(&bar[XB_TOPGEN]) == tg, bar);
;             asm volatile("s_waitcnt vmcnt(0)" ::: "memory");
;         } else {
;             __builtin_amdgcn_fence(__ATOMIC_ACQUIRE, "agent");
;             XB_SPIN(xb_ld(&bar[XB_TOPGEN]) == gen, bar);
.LBB0_370:
	s_or_b64 exec, exec, s[4:5]
	v_cvt_f32_u32_e32 v4, v2
	s_waitcnt vmcnt(0)
	v_readfirstlane_b32 s4, v3
	v_sub_u32_e32 v3, 0, v2
	v_rcp_iflag_f32_e32 v4, v4
	v_add_u32_e32 v5, s4, v1
	v_mul_f32_e32 v4, 0x4f7ffffe, v4
	v_cvt_u32_f32_e32 v4, v4
	v_mul_lo_u32 v1, v3, v4
	v_mul_hi_u32 v1, v4, v1
	v_add_u32_e32 v1, v4, v1
	v_mul_hi_u32 v1, v5, v1
	v_mul_lo_u32 v3, v1, v2
	v_sub_u32_e32 v3, v5, v3
	v_add_u32_e32 v4, 1, v1
	v_cmp_ge_u32_e32 vcc, v3, v2
	s_nop 1
	v_cndmask_b32_e32 v1, v1, v4, vcc
	v_sub_u32_e32 v4, v3, v2
	v_cndmask_b32_e32 v3, v3, v4, vcc
	v_add_u32_e32 v4, 1, v1
	v_cmp_ge_u32_e32 vcc, v3, v2
	v_add_u32_e32 v3, 1, v5
	s_nop 0
	v_cndmask_b32_e32 v1, v1, v4, vcc
	v_mul_lo_u32 v4, v2, v1
	v_add_u32_e32 v2, v4, v2
	v_cmp_ne_u32_e32 vcc, v3, v2
	s_and_saveexec_b64 s[4:5], vcc
	s_xor_b64 s[4:5], exec, s[4:5]
	s_cbranch_execz .LBB0_384
	s_waitcnt lgkmcnt(0)
	v_add_u32_e32 v2, 1, v1
	v_mul_lo_u32 v2, v2, v0
	v_mov_b32_e32 v0, 0x3000
	buffer_inv sc1
	global_load_dword v0, v0, s[2:3] offset:1024 sc1
	s_add_u32 s8, s2, 0x3400
	s_addc_u32 s9, s3, 0
	s_waitcnt vmcnt(0)
	v_cmp_lt_u32_e32 vcc, v0, v2
	s_and_saveexec_b64 s[6:7], vcc
	s_cbranch_execz .LBB0_383
	s_mov_b32 s20, 1
	s_mov_b64 s[10:11], 0
	s_branch .LBB0_374

; __device__ __forceinline__ unsigned xb_ld(unsigned* p)              { return __hip_atomic_load(p, __ATOMIC_RELAXED, __HIP_MEMORY_SCOPE_AGENT); }
; #define XB_SPIN(cond, bar) do { unsigned _sp = 0; while (cond) { __builtin_amdgcn_s_sleep(1); \
;     if ((++_sp & 255u) == 0u) { if (xb_ld(&(bar)[XB_TMO])) break; if (_sp > XB_SPIN_CAP) { atomicAdd(&(bar)[XB_TMO], 1u); break; } } } } while (0)
; __device__ __forceinline__ void xcd_barrier(const XcdBarrier& b, const int wv) {
;     ...
;             else XB_SPIN(xb_ld(&bar[XB_TOPGEN]) == tg, bar);
;             asm volatile("s_waitcnt vmcnt(0)" ::: "memory");
;         } else {
;             __builtin_amdgcn_fence(__ATOMIC_ACQUIRE, "agent");
;             XB_SPIN(xb_ld(&bar[XB_TOPGEN]) == gen, bar);
.LBB0_376:
	global_load_dword v0, v65, s[8:9] sc1
	s_add_i32 s20, s20, 1
	s_mov_b64 s[16:17], -1
	s_waitcnt vmcnt(0)
	v_cmp_ge_u32_e32 vcc, v0, v2
	s_orn2_b64 s[14:15], vcc, exec
	s_branch .LBB0_373

; __device__ __forceinline__ unsigned xb_ld(unsigned* p)              { return __hip_atomic_load(p, __ATOMIC_RELAXED, __HIP_MEMORY_SCOPE_AGENT); }
; __device__ __forceinline__ unsigned xb_add(unsigned* p, unsigned v) { return __hip_atomic_fetch_add(p, v, __ATOMIC_RELAXED, __HIP_MEMORY_SCOPE_AGENT); }
; #define XB_SPIN(cond, bar) do { unsigned _sp = 0; while (cond) { __builtin_amdgcn_s_sleep(1); \
;     if ((++_sp & 255u) == 0u) { if (xb_ld(&(bar)[XB_TMO])) break; if (_sp > XB_SPIN_CAP) { atomicAdd(&(bar)[XB_TMO], 1u); break; } } } } while (0)
; __device__ __forceinline__ void xcd_barrier(const XcdBarrier& b, const int wv) {
;     ...
;         const unsigned old = xb_add(&bar[XB_XSUB(bx)], 1u);
;         const unsigned gen = old / nloc;
;         if (old + 1u == (gen + 1u) * nloc) {
;             __builtin_amdgcn_fence(__ATOMIC_RELEASE, "agent");
;             asm volatile("s_waitcnt vmcnt(0)" ::: "memory");
;             const unsigned og = xb_add(&bar[XB_TOP], 1u);
;             const unsigned tg = og / nx;
;             __builtin_amdgcn_fence(__ATOMIC_ACQUIRE, "agent");
;             if (og + 1u == (tg + 1u) * nx) xb_add(&bar[XB_TOPGEN], 1u);
;             else XB_SPIN(xb_ld(&bar[XB_TOPGEN]) == tg, bar);
;             asm volatile("s_waitcnt vmcnt(0)" ::: "memory");
.LBB0_387:
	s_or_b64 exec, exec, s[6:7]
	v_cvt_f32_u32_e32 v3, v0
	s_waitcnt vmcnt(0)
	v_readfirstlane_b32 s4, v2
	s_add_u32 s6, s2, 0x3400
	s_addc_u32 s7, s3, 0
	v_rcp_iflag_f32_e32 v3, v3
	v_add_u32_e32 v1, s4, v1
	s_mov_b64 s[8:9], 0
	buffer_inv sc1
	v_mul_f32_e32 v2, 0x4f7ffffe, v3
	v_cvt_u32_f32_e32 v2, v2
	v_sub_u32_e32 v3, 0, v0
	v_mul_lo_u32 v3, v3, v2
	v_mul_hi_u32 v3, v2, v3
	v_add_u32_e32 v2, v2, v3
	v_mul_hi_u32 v2, v1, v2
	v_mul_lo_u32 v3, v2, v0
	v_sub_u32_e32 v3, v1, v3
	v_add_u32_e32 v4, 1, v2
	v_cmp_ge_u32_e32 vcc, v3, v0
	v_add_u32_e32 v1, 1, v1
	s_nop 0
	v_cndmask_b32_e32 v2, v2, v4, vcc
	v_sub_u32_e32 v4, v3, v0
	v_cndmask_b32_e32 v3, v3, v4, vcc
	v_add_u32_e32 v4, 1, v2
	v_cmp_ge_u32_e32 vcc, v3, v0
	s_nop 1
	v_cndmask_b32_e32 v2, v2, v4, vcc
	v_mul_lo_u32 v3, v0, v2
	v_add_u32_e32 v0, v3, v0
	v_cmp_ne_u32_e32 vcc, v1, v0
	v_mov_b32_e32 v3, v0
	v_mov_b64_e32 v[0:1], s[6:7]
	s_and_saveexec_b64 s[4:5], vcc
	s_cbranch_execz .LBB0_399
	global_load_dword v0, v65, s[6:7] sc1
	s_mov_b64 s[12:13], 0
	s_waitcnt vmcnt(0)
	v_cmp_lt_u32_e32 vcc, v0, v3
	s_and_saveexec_b64 s[10:11], vcc
	s_cbranch_execz .LBB0_398
	s_add_u32 s8, s2, 0x200
	s_addc_u32 s9, s3, 0
	s_mov_b32 s20, 1
	s_mov_b64 s[2:3], 0
	s_branch .LBB0_391

; __device__ __forceinline__ unsigned xb_ld(unsigned* p)              { return __hip_atomic_load(p, __ATOMIC_RELAXED, __HIP_MEMORY_SCOPE_AGENT); }
; #define XB_SPIN(cond, bar) do { unsigned _sp = 0; while (cond) { __builtin_amdgcn_s_sleep(1); \
;     if ((++_sp & 255u) == 0u) { if (xb_ld(&(bar)[XB_TMO])) break; if (_sp > XB_SPIN_CAP) { atomicAdd(&(bar)[XB_TMO], 1u); break; } } } } while (0)
; __device__ __forceinline__ void xcd_barrier(const XcdBarrier& b, const int wv) {
;     ...
;             else XB_SPIN(xb_ld(&bar[XB_TOPGEN]) == tg, bar);
.LBB0_393:
	global_load_dword v0, v65, s[6:7] sc1
	s_add_i32 s20, s20, 1
	s_mov_b64 s[16:17], -1
	s_waitcnt vmcnt(0)
	v_cmp_ge_u32_e32 vcc, v0, v3
	s_orn2_b64 s[14:15], vcc, exec
	s_branch .LBB0_390
